# baseline (speedup 1.0000x reference)
.LBB0_3:
	s_load_dwordx8 s[8:15], s[0:1], 0x0
	v_and_b32_e32 v199, 15, v0
	v_lshrrev_b32_e32 v206, 4, v1
	s_cmpk_gt_u32 s38, 0x17f
	v_lshlrev_b32_e32 v205, 2, v206
	v_lshlrev_b32_e32 v194, 4, v206
	s_mul_i32 s37, s3, 0xc8
	v_lshl_or_b32 v204, s36, 4, v199
	s_cbranch_scc0 .LBB0_52
	s_add_i32 s39, s36, -6
	s_lshl_b32 s4, s33, 7
	s_waitcnt lgkmcnt(0)
	s_add_u32 s40, s20, s4
	s_addc_u32 s41, s21, 0
	s_add_u32 s6, s24, s4
	s_addc_u32 s7, s25, 0
	s_lshl_b32 s24, s39, 4
	v_or_b32_e32 v131, s24, v199
	v_min_u32_e32 v2, 0xc7, v131
	v_add_u32_e32 v2, s37, v2
	v_ashrrev_i32_e32 v3, 31, v2
	v_lshlrev_b64 v[2:3], 2, v[2:3]
	s_add_i32 s21, s36, -4
	v_lshl_add_u64 v[4:5], s[8:9], 0, v[2:3]
	v_lshl_add_u64 v[2:3], s[10:11], 0, v[2:3]
	v_lshl_or_b32 v201, s21, 4, v199
	global_load_dword v35, v[2:3], off
	v_min_u32_e32 v2, 0xc7, v201
	v_add_u32_e32 v2, s37, v2
	v_ashrrev_i32_e32 v3, 31, v2
	v_lshlrev_b64 v[2:3], 2, v[2:3]
	global_load_dword v34, v[4:5], off
	v_lshl_add_u64 v[4:5], s[8:9], 0, v[2:3]
	v_lshl_add_u64 v[2:3], s[10:11], 0, v[2:3]
	global_load_dword v36, v[4:5], off
	global_load_dword v37, v[2:3], off
	v_mov_b32_e32 v195, 0
	v_lshlrev_b32_e32 v42, 4, v0
	v_mov_b32_e32 v43, v195
	s_movk_i32 s20, 0x2000
	v_lshl_add_u64 v[10:11], s[34:35], 0, v[42:43]
	v_add_co_u32_e32 v20, vcc, s20, v10
	s_movk_i32 s42, 0x4000
	s_nop 0
	v_addc_co_u32_e32 v21, vcc, 0, v11, vcc
	v_lshlrev_b32_e32 v6, 6, v0
	v_add_co_u32_e32 v22, vcc, s42, v10
	s_movk_i32 s43, 0x6000
	v_and_b32_e32 v6, 0x7e00, v6
	v_mov_b32_e32 v7, v195
	v_addc_co_u32_e32 v23, vcc, 0, v11, vcc
	s_mov_b32 s5, 0
	v_mov_b32_e32 v9, v195
	v_lshl_add_u64 v[12:13], s[18:19], 0, v[6:7]
	v_or_b32_e32 v8, 0x8000, v6
	v_lshl_add_u64 v[6:7], s[22:23], 0, v[6:7]
	v_add_co_u32_e32 v24, vcc, s43, v10
	global_load_dwordx4 v[118:121], v194, s[40:41]
	global_load_dwordx4 v[114:117], v194, s[40:41] offset:64
	v_addc_co_u32_e32 v25, vcc, 0, v11, vcc
	v_lshl_add_u64 v[26:27], v[12:13], 0, s[4:5]
	v_lshl_add_u64 v[28:29], s[18:19], 0, v[8:9]
	v_lshl_add_u64 v[30:31], v[6:7], 0, s[4:5]
	v_lshl_add_u64 v[32:33], s[22:23], 0, v[8:9]
	v_and_b32_e32 v18, 0x70, v42
	v_mov_b32_e32 v19, v195
	v_lshl_add_u64 v[38:39], v[26:27], 0, v[18:19]
	v_lshl_add_u64 v[20:21], v[28:29], 0, s[4:5]
	v_lshl_add_u64 v[22:23], v[32:33], 0, s[4:5]
	v_lshl_add_u64 v[40:41], v[30:31], 0, v[18:19]
	global_load_dwordx4 v[126:129], v194, s[6:7]
	global_load_dwordx4 v[122:125], v194, s[6:7] offset:64
	v_lshl_add_u64 v[44:45], v[20:21], 0, v[18:19]
	v_lshl_add_u64 v[46:47], v[22:23], 0, v[18:19]
	s_movk_i32 s25, 0x2710
	s_add_i32 s20, s36, -2
	v_lshl_or_b32 v207, s20, 4, v199
	v_min_u32_e32 v43, 0xc7, v207
	v_and_b32_e32 v42, 48, v42
	v_lshlrev_b32_e32 v48, 2, v0
	s_waitcnt vmcnt(6)
	v_mad_u64_u32 v[34:35], s[4:5], v35, s25, v[34:35]
	v_ashrrev_i32_e32 v35, 31, v34
	v_lshlrev_b64 v[34:35], 9, v[34:35]
	s_waitcnt vmcnt(4)
	v_mad_u64_u32 v[36:37], s[4:5], v37, s25, v[36:37]
	v_ashrrev_i32_e32 v37, 31, v36
	v_lshlrev_b64 v[44:45], 9, v[36:37]
	v_lshl_add_u64 v[34:35], s[14:15], 0, v[34:35]
	v_lshl_add_u64 v[44:45], s[14:15], 0, v[44:45]
	v_lshl_add_u64 v[46:47], v[34:35], 0, v[194:195]
	v_lshl_add_u64 v[44:45], v[44:45], 0, v[194:195]
	global_load_dwordx4 v[34:37], v[46:47], off
	global_load_dwordx4 v[38:41], v[46:47], off offset:64
	global_load_dwordx4 v[54:57], v[46:47], off offset:128
	global_load_dwordx4 v[82:85], v[46:47], off offset:192
	global_load_dwordx4 v[86:89], v[46:47], off offset:256
	global_load_dwordx4 v[90:93], v[46:47], off offset:320
	global_load_dwordx4 v[94:97], v[46:47], off offset:384
	global_load_dwordx4 v[98:101], v[46:47], off offset:448
	global_load_dwordx4 v[158:161], v[44:45], off
	global_load_dwordx4 v[154:157], v[44:45], off offset:64
	global_load_dwordx4 v[150:153], v[44:45], off offset:128
	global_load_dwordx4 v[146:149], v[44:45], off offset:192
	global_load_dwordx4 v[66:69], v[44:45], off offset:256
	global_load_dwordx4 v[70:73], v[44:45], off offset:320
	global_load_dwordx4 v[74:77], v[44:45], off offset:384
	global_load_dwordx4 v[78:81], v[44:45], off offset:448
	v_add_u32_e32 v44, s37, v43
	v_ashrrev_i32_e32 v45, 31, v44
	v_lshlrev_b64 v[44:45], 2, v[44:45]
	v_lshl_add_u64 v[46:47], s[8:9], 0, v[44:45]
	v_lshl_add_u64 v[44:45], s[10:11], 0, v[44:45]
	global_load_dword v140, v[46:47], off
	global_load_dword v135, v[44:45], off
	v_min_u32_e32 v43, 0xc7, v204
	v_add_u32_e32 v44, s37, v43
	v_ashrrev_i32_e32 v45, 31, v44
	s_add_i32 s4, s24, 0x80
	v_lshlrev_b64 v[44:45], 2, v[44:45]
	v_or_b32_e32 v43, s4, v199
	v_lshl_add_u64 v[46:47], s[8:9], 0, v[44:45]
	v_lshl_add_u64 v[44:45], s[10:11], 0, v[44:45]
	v_min_u32_e32 v43, 0xc7, v43
	global_load_dword v133, v[44:45], off
	v_add_u32_e32 v44, s37, v43
	v_ashrrev_i32_e32 v45, 31, v44
	v_lshlrev_b64 v[44:45], 2, v[44:45]
	global_load_dword v130, v[46:47], off
	v_lshl_add_u64 v[46:47], s[8:9], 0, v[44:45]
	v_lshl_add_u64 v[44:45], s[10:11], 0, v[44:45]
	global_load_dword v134, v[44:45], off
	v_lshlrev_b32_e32 v45, 3, v0
	v_lshrrev_b32_e32 v43, 5, v0
	v_and_b32_e32 v44, 4, v0
	v_and_b32_e32 v45, 0xc0, v45
	v_or3_b32 v42, v42, v43, v45
	v_lshlrev_b32_e32 v43, 1, v44
	s_waitcnt vmcnt(32)
	v_cvt_pk_f16_f32 v2, v2, v3
	v_cvt_pk_f16_f32 v3, v4, v5
	v_lshl_or_b32 v42, v42, 4, v43
	s_waitcnt vmcnt(29)
	v_cvt_pk_f16_f32 v4, v6, v7
	v_cvt_pk_f16_f32 v5, v8, v9
	s_waitcnt vmcnt(28)
	v_cvt_pk_f16_f32 v2, v10, v11
	v_cvt_pk_f16_f32 v3, v12, v13
	s_waitcnt vmcnt(27)
	v_cvt_pk_f16_f32 v4, v14, v15
	v_cvt_pk_f16_f32 v5, v16, v17
	v_lshrrev_b32_e32 v4, 2, v0
	v_lshrrev_b32_e32 v2, 1, v0
	v_lshrrev_b32_e32 v3, 4, v0
	v_and_b32_e32 v4, 6, v4
	v_and_b32_e32 v2, 48, v2
	v_and_or_b32 v3, v3, 8, v4
	v_lshrrev_b32_e32 v4, 8, v0
	v_and_or_b32 v2, v48, 12, v2
	v_or_b32_e32 v4, v4, v44
	s_waitcnt vmcnt(24)
	v_cvt_f16_f32_e32 v5, v18
	v_lshlrev_b32_e32 v4, 10, v4
	v_lshlrev_b32_e32 v2, 4, v2
	v_or3_b32 v2, v2, v4, v3
	v_cvt_f16_f32_e32 v3, v19
	v_cvt_f16_f32_e32 v4, v20
	v_add_u32_e32 v2, 0x10a00, v2
	v_cvt_f16_f32_e32 v6, v21
	global_load_dword v132, v[46:47], off
	s_waitcnt vmcnt(24)
	v_cvt_f16_f32_e32 v3, v22
	v_cvt_f16_f32_e32 v4, v23
	v_cvt_f16_f32_e32 v5, v24
	v_cvt_f16_f32_e32 v6, v25
	s_waitcnt vmcnt(23)
	v_cvt_f16_f32_e32 v3, v26
	v_cvt_f16_f32_e32 v4, v27
	v_cvt_f16_f32_e32 v5, v28
	v_cvt_f16_f32_e32 v6, v29
	s_waitcnt vmcnt(22)
	v_cvt_f16_f32_e32 v3, v30
	v_cvt_f16_f32_e32 v4, v31
	v_cvt_f16_f32_e32 v5, v32
	v_cvt_f16_f32_e32 v6, v33
	v_mov_b32_e32 v2, 0x10a00
	s_waitcnt lgkmcnt(0)
	s_barrier
	v_lshl_add_u32 v141, v1, 4, v2
	ds_read_b128 v[6:9], v141
	ds_read_b128 v[2:5], v141 offset:1024
	ds_read_b128 v[10:13], v141 offset:4096
	ds_read_b128 v[14:17], v141 offset:8192
	s_waitcnt vmcnt(21)
	v_cvt_pk_f16_f32 v102, v34, v35
	v_cvt_pk_f16_f32 v103, v36, v37
	s_waitcnt vmcnt(20)
	v_cvt_pk_f16_f32 v104, v38, v39
	v_cvt_pk_f16_f32 v105, v40, v41
	ds_read_b128 v[26:29], v141 offset:2048
	ds_read_b128 v[18:21], v141 offset:3072
	ds_read_b128 v[46:49], v141 offset:5120
	ds_read_b128 v[58:61], v141 offset:12288
	s_waitcnt lgkmcnt(7)
	v_mfma_f32_16x16x32_f16 v[38:41], v[6:9], v[102:105], 0
	s_waitcnt vmcnt(19)
	v_cvt_pk_f16_f32 v136, v54, v55
	v_cvt_pk_f16_f32 v137, v56, v57
	s_waitcnt vmcnt(18)
	v_cvt_pk_f16_f32 v138, v82, v83
	s_waitcnt lgkmcnt(5)
	v_mfma_f32_16x16x32_f16 v[106:109], v[10:13], v[102:105], 0
	v_cvt_pk_f16_f32 v139, v84, v85
	ds_read_b128 v[34:37], v141 offset:6144
	ds_read_b128 v[22:25], v141 offset:7168
	ds_read_b128 v[50:53], v141 offset:9216
	ds_read_b128 v[42:45], v141 offset:10240
	ds_read_b128 v[30:33], v141 offset:11264
	ds_read_b128 v[62:65], v141 offset:13312
	v_mfma_f32_16x16x32_f16 v[82:85], v[2:5], v[136:139], v[38:41]
	ds_read_b128 v[54:57], v141 offset:14336
	s_nop 1
	ds_read_b128 v[38:41], v141 offset:15360
	s_waitcnt vmcnt(4)
	v_mad_u64_u32 v[144:145], s[4:5], v135, s25, v[140:141]
	s_waitcnt lgkmcnt(12)
	v_mfma_f32_16x16x32_f16 v[110:113], v[14:17], v[102:105], 0
	v_cvt_pk_f16_f32 v140, v86, v87
	v_cvt_pk_f16_f32 v141, v88, v89
	v_cvt_pk_f16_f32 v142, v90, v91
	s_waitcnt lgkmcnt(8)
	v_mfma_f32_16x16x32_f16 v[102:105], v[58:61], v[102:105], 0
	v_cvt_pk_f16_f32 v143, v92, v93
	v_cvt_pk_f16_f32 v164, v98, v99
	v_cvt_pk_f16_f32 v165, v100, v101
	v_mfma_f32_16x16x32_f16 v[106:109], v[46:49], v[136:139], v[106:109]
	s_add_i32 s4, s24, 0xa0
	v_ashrrev_i32_e32 v145, 31, v144
	v_cvt_pk_f16_f32 v162, v94, v95
	v_mfma_f32_16x16x32_f16 v[98:101], v[26:29], v[140:143], v[82:85]
	v_cvt_pk_f16_f32 v163, v96, v97
	s_waitcnt lgkmcnt(5)
	v_mfma_f32_16x16x32_f16 v[86:89], v[50:53], v[136:139], v[110:113]
	v_lshlrev_b64 v[82:83], 9, v[144:145]
	v_lshl_add_u64 v[82:83], s[14:15], 0, v[82:83]
	v_lshl_add_u64 v[94:95], v[82:83], 0, v[194:195]
	s_waitcnt lgkmcnt(2)
	v_mfma_f32_16x16x32_f16 v[102:105], v[62:65], v[136:139], v[102:105]
	global_load_dwordx4 v[190:193], v[94:95], off
	global_load_dwordx4 v[186:189], v[94:95], off offset:64
	global_load_dwordx4 v[182:185], v[94:95], off offset:128
	global_load_dwordx4 v[178:181], v[94:95], off offset:192
	v_mfma_f32_16x16x32_f16 v[110:113], v[34:37], v[140:143], v[106:109]
	s_nop 2
	v_or_b32_e32 v106, s4, v199
	v_min_u32_e32 v135, 0xc7, v106
	v_mfma_f32_16x16x32_f16 v[106:109], v[18:21], v[162:165], v[98:101]
	s_movk_i32 s4, 0xc8
	v_cmp_gt_u32_e32 vcc, s4, v131
	s_nop 0
	v_add_u32_e32 v98, s37, v135
	v_ashrrev_i32_e32 v99, 31, v98
	v_mfma_f32_16x16x32_f16 v[136:139], v[42:45], v[140:143], v[86:89]
	global_load_dwordx4 v[82:85], v[94:95], off offset:256
	s_nop 1
	global_load_dwordx4 v[86:89], v[94:95], off offset:320
	global_load_dwordx4 v[90:93], v[94:95], off offset:384
	s_nop 0
	global_load_dwordx4 v[94:97], v[94:95], off offset:448
	s_waitcnt lgkmcnt(1)
	v_mfma_f32_16x16x32_f16 v[102:105], v[54:57], v[140:143], v[102:105]
	v_lshlrev_b64 v[140:141], 2, v[98:99]
	v_mfma_f32_16x16x32_f16 v[98:101], v[22:25], v[162:165], v[110:113]
	s_nop 2
	v_lshl_add_u64 v[110:111], s[8:9], 0, v[140:141]
	v_lshl_add_u64 v[140:141], s[10:11], 0, v[140:141]
	global_load_dword v200, v[110:111], off
	global_load_dword v208, v[140:141], off
	v_mfma_f32_16x16x32_f16 v[110:113], v[30:33], v[162:165], v[136:139]
	s_waitcnt lgkmcnt(0)
	v_mfma_f32_16x16x32_f16 v[102:105], v[38:41], v[162:165], v[102:105]
	s_and_saveexec_b64 s[4:5], vcc
	s_cbranch_execz .LBB0_6
	v_mul_f32_e32 v135, 0xbfb8aa3b, v118
	v_fmac_f32_e32 v135, 0xbfb8aa3b, v106
	v_exp_f32_e32 v106, v135
	v_mul_f32_e32 v135, 0x4038aa3b, v126
	v_fmac_f32_e32 v135, 0x4038aa3b, v110
	v_exp_f32_e32 v110, v135
	v_add_f32_e32 v106, 1.0, v106
	v_rcp_f32_e32 v135, v106
	s_movk_i32 s6, 0xca0
	v_add_f32_e32 v106, 1.0, v110
	v_mul_f32_e32 v110, 0xbfb8aa3b, v114
	v_fmac_f32_e32 v110, 0xbfb8aa3b, v98
	v_exp_f32_e32 v98, v110
	v_mul_f32_e32 v110, 0x4038aa3b, v122
	v_fmac_f32_e32 v110, 0x4038aa3b, v102
	v_exp_f32_e32 v102, v110
	v_add_f32_e32 v98, 1.0, v98
	v_rcp_f32_e32 v110, v98
	v_rcp_f32_e32 v106, v106
	v_add_f32_e32 v98, 1.0, v102
	v_mul_f32_e32 v102, 0xbfb8aa3b, v119
	v_fmac_f32_e32 v102, 0xbfb8aa3b, v107
	v_mul_f32_e32 v107, 0x4038aa3b, v127
	v_exp_f32_e32 v102, v102
	v_fmac_f32_e32 v107, 0x4038aa3b, v111
	v_exp_f32_e32 v107, v107
	v_rcp_f32_e32 v98, v98
	v_add_f32_e32 v102, 1.0, v102
	v_rcp_f32_e32 v111, v102
	v_add_f32_e32 v102, 1.0, v107
	v_rcp_f32_e32 v107, v102
	v_mul_f32_e32 v102, 0xbfb8aa3b, v115
	v_fmac_f32_e32 v102, 0xbfb8aa3b, v99
	v_exp_f32_e32 v99, v102
	v_mul_f32_e32 v102, 0x4038aa3b, v123
	v_fmac_f32_e32 v102, 0x4038aa3b, v103
	v_exp_f32_e32 v136, v102
	v_pk_fma_f32 v[102:103], v[106:107], -2.0, 1.0 op_sel_hi:[1,0,0]
	v_mul_f32_e32 v106, 0xbfb8aa3b, v120
	v_fmac_f32_e32 v106, 0xbfb8aa3b, v108
	v_mul_f32_e32 v107, 0x4038aa3b, v128
	v_exp_f32_e32 v106, v106
	v_fmac_f32_e32 v107, 0x4038aa3b, v112
	v_exp_f32_e32 v107, v107
	v_add_f32_e32 v99, 1.0, v99
	v_add_f32_e32 v106, 1.0, v106
	v_rcp_f32_e32 v108, v106
	v_add_f32_e32 v106, 1.0, v107
	v_mul_f32_e32 v107, 0xbfb8aa3b, v116
	v_fmac_f32_e32 v107, 0xbfb8aa3b, v100
	v_exp_f32_e32 v100, v107
	v_mul_f32_e32 v107, 0x4038aa3b, v124
	v_fmac_f32_e32 v107, 0x4038aa3b, v104
	v_exp_f32_e32 v104, v107
	v_add_f32_e32 v100, 1.0, v100
	v_rcp_f32_e32 v112, v100
	v_mul_f32_e32 v107, 0x4038aa3b, v129
	v_add_f32_e32 v100, 1.0, v104
	v_mul_f32_e32 v104, 0xbfb8aa3b, v121
	v_fmac_f32_e32 v104, 0xbfb8aa3b, v109
	v_exp_f32_e32 v104, v104
	v_fmac_f32_e32 v107, 0x4038aa3b, v113
	v_exp_f32_e32 v107, v107
	v_rcp_f32_e32 v106, v106
	v_add_f32_e32 v104, 1.0, v104
	v_rcp_f32_e32 v109, v104
	v_add_f32_e32 v104, 1.0, v107
	v_rcp_f32_e32 v107, v104
	v_mul_f32_e32 v104, 0x4038aa3b, v125
	v_fmac_f32_e32 v104, 0x4038aa3b, v105
	v_mul_f32_e32 v105, 0xbfb8aa3b, v117
	v_exp_f32_e32 v104, v104
	v_fmac_f32_e32 v105, 0xbfb8aa3b, v101
	v_exp_f32_e32 v113, v105
	v_rcp_f32_e32 v137, v99
	v_add_f32_e32 v99, 1.0, v136
	v_add_f32_e32 v101, 1.0, v104
	v_rcp_f32_e32 v99, v99
	v_rcp_f32_e32 v100, v100
	v_rcp_f32_e32 v101, v101
	v_pk_fma_f32 v[104:105], v[106:107], -2.0, 1.0 op_sel_hi:[1,0,0]
	v_add_f32_e32 v106, 1.0, v113
	v_rcp_f32_e32 v113, v106
	v_cvt_pk_f16_f32 v107, v102, v103
	v_lshlrev_b32_e32 v102, 3, v131
	v_cvt_pk_f16_f32 v106, v135, v111
	v_mad_u32_u24 v111, v206, s6, v102
	v_pk_fma_f32 v[98:99], v[98:99], -2.0, 1.0 op_sel_hi:[1,0,0]
	v_pk_fma_f32 v[100:101], v[100:101], -2.0, 1.0 op_sel_hi:[1,0,0]
	v_cvt_pk_f16_f32 v102, v108, v109
	v_cvt_pk_f16_f32 v103, v104, v105
	v_add_u32_e32 v104, 0x6400, v111
	ds_write2_b64 v104, v[106:107], v[102:103] offset0:32 offset1:234
	v_cvt_pk_f16_f32 v102, v110, v137
	v_cvt_pk_f16_f32 v103, v98, v99
	v_cvt_pk_f16_f32 v98, v112, v113
	v_cvt_pk_f16_f32 v99, v100, v101
	v_add_u32_e32 v100, 0x9600, v111
	ds_write2_b64 v100, v[102:103], v[98:99] offset0:48 offset1:250

.LBB0_52:
	s_and_b64 vcc, exec, s[4:5]
	s_cbranch_vccz .LBB0_77
	s_add_i32 s42, s36, -4
	s_waitcnt vmcnt(2)
	v_lshl_or_b32 v87, s42, 4, v199
	s_waitcnt lgkmcnt(0)
	s_add_i32 s24, s36, -2
	v_add_u32_e32 v2, s37, v87
	v_lshl_or_b32 v179, s24, 4, v199
	v_ashrrev_i32_e32 v3, 31, v2
	v_add_u32_e32 v6, s37, v179
	v_lshl_add_u64 v[4:5], v[2:3], 2, s[8:9]
	v_ashrrev_i32_e32 v7, 31, v6
	v_lshl_add_u64 v[6:7], v[6:7], 2, s[8:9]
	global_load_dword v36, v[4:5], off
	global_load_dword v38, v[6:7], off
	v_lshlrev_b32_e32 v40, 4, v0
	v_mov_b32_e32 v41, 0
	s_movk_i32 s4, 0x2000
	v_lshl_add_u64 v[16:17], s[34:35], 0, v[40:41]
	v_add_co_u32_e32 v18, vcc, s4, v16
	s_movk_i32 s5, 0x4000
	s_nop 0
	v_addc_co_u32_e32 v19, vcc, 0, v17, vcc
	v_add_u32_e32 v4, s37, v204
	v_add_co_u32_e32 v20, vcc, s5, v16
	s_movk_i32 s6, 0x6000
	v_ashrrev_i32_e32 v5, 31, v4
	v_addc_co_u32_e32 v21, vcc, 0, v17, vcc
	v_lshl_add_u64 v[8:9], v[4:5], 2, s[8:9]
	v_add_co_u32_e32 v16, vcc, s6, v16
	global_load_dword v42, v[8:9], off
	v_addc_co_u32_e32 v17, vcc, 0, v17, vcc
	v_lshlrev_b32_e32 v3, 6, v0
	v_and_b32_e32 v24, 0x7e00, v3
	v_mov_b32_e32 v25, v41
	s_mov_b32 s5, 0
	s_lshl_b32 s4, s33, 7
	v_lshl_add_u64 v[20:21], s[18:19], 0, v[24:25]
	v_and_b32_e32 v28, 0x70, v40
	v_mov_b32_e32 v29, v41
	v_lshl_add_u64 v[20:21], v[20:21], 0, s[4:5]
	v_lshl_add_u64 v[20:21], v[20:21], 0, v[28:29]
	v_mov_b32_e32 v27, v41
	v_or_b32_e32 v26, 0x8000, v24
	v_lshl_add_u64 v[24:25], s[22:23], 0, v[24:25]
	v_lshl_add_u64 v[30:31], s[18:19], 0, v[26:27]
	v_lshl_add_u64 v[32:33], v[24:25], 0, s[4:5]
	v_lshl_add_u64 v[24:25], v[30:31], 0, s[4:5]
	v_lshl_add_u64 v[24:25], v[24:25], 0, v[28:29]
	v_lshl_add_u64 v[34:35], s[22:23], 0, v[26:27]
	v_lshl_add_u64 v[44:45], v[32:33], 0, v[28:29]
	v_lshl_add_u64 v[30:31], v[34:35], 0, s[4:5]
	v_lshl_add_u64 v[46:47], v[30:31], 0, v[28:29]
	s_add_i32 s39, s36, 2
	s_waitcnt vmcnt(3)
	v_mov_b32_e32 v195, v41
	s_lshl_b32 s41, s39, 4
	s_add_i32 s4, s41, s37
	v_lshlrev_b32_e32 v3, 2, v0
	s_load_dwordx2 s[20:21], s[0:1], 0x70
	s_cmp_eq_u32 s33, 0
	s_waitcnt vmcnt(2)
	v_ashrrev_i32_e32 v37, 31, v36
	s_waitcnt vmcnt(1)
	v_ashrrev_i32_e32 v39, 31, v38
	v_lshlrev_b64 v[36:37], 9, v[36:37]
	v_lshlrev_b64 v[38:39], 9, v[38:39]
	v_lshl_add_u64 v[36:37], s[12:13], 0, v[36:37]
	v_lshl_add_u64 v[38:39], s[12:13], 0, v[38:39]
	v_lshl_add_u64 v[36:37], v[36:37], 0, v[194:195]
	v_lshl_add_u64 v[38:39], v[38:39], 0, v[194:195]
	global_load_dwordx4 v[66:69], v[36:37], off
	global_load_dwordx4 v[70:73], v[36:37], off offset:64
	global_load_dwordx4 v[74:77], v[36:37], off offset:128
	global_load_dwordx4 v[102:105], v[36:37], off offset:192
	global_load_dwordx4 v[110:113], v[36:37], off offset:256
	global_load_dwordx4 v[162:165], v[36:37], off offset:320
	global_load_dwordx4 v[166:169], v[36:37], off offset:384
	global_load_dwordx4 v[170:173], v[36:37], off offset:448
	global_load_dwordx4 v[142:145], v[38:39], off
	global_load_dwordx4 v[138:141], v[38:39], off offset:64
	global_load_dwordx4 v[134:137], v[38:39], off offset:128
	global_load_dwordx4 v[130:133], v[38:39], off offset:192
	global_load_dwordx4 v[122:125], v[38:39], off offset:256
	global_load_dwordx4 v[118:121], v[38:39], off offset:320
	global_load_dwordx4 v[90:93], v[38:39], off offset:384
	global_load_dwordx4 v[94:97], v[38:39], off offset:448
	v_add_u32_e32 v36, s4, v199
	v_add_u32_e32 v38, 0x80, v2
	v_ashrrev_i32_e32 v37, 31, v36
	v_ashrrev_i32_e32 v39, 31, v38
	v_lshl_add_u64 v[36:37], v[36:37], 2, s[8:9]
	v_lshl_add_u64 v[38:39], v[38:39], 2, s[8:9]
	global_load_dword v88, v[36:37], off
	global_load_dword v86, v[38:39], off
	v_lshlrev_b32_e32 v39, 3, v0
	v_lshrrev_b32_e32 v36, 5, v0
	v_and_b32_e32 v37, 4, v0
	v_and_b32_e32 v38, 48, v40
	v_and_b32_e32 v39, 0xc0, v39
	v_or3_b32 v36, v38, v36, v39
	v_lshlrev_b32_e32 v38, 1, v37
	s_waitcnt vmcnt(25)
	v_cvt_pk_f16_f32 v4, v4, v5
	v_cvt_pk_f16_f32 v5, v6, v7
	v_lshl_or_b32 v36, v36, 4, v38
	s_waitcnt vmcnt(24)
	v_cvt_pk_f16_f32 v6, v8, v9
	v_cvt_pk_f16_f32 v7, v10, v11
	s_waitcnt vmcnt(23)
	v_cvt_pk_f16_f32 v4, v12, v13
	v_cvt_pk_f16_f32 v5, v14, v15
	s_waitcnt vmcnt(22)
	v_cvt_pk_f16_f32 v6, v16, v17
	v_cvt_pk_f16_f32 v7, v18, v19
	v_lshrrev_b32_e32 v4, 1, v0
	v_and_b32_e32 v4, 48, v4
	v_lshrrev_b32_e32 v5, 2, v0
	v_and_or_b32 v3, v3, 12, v4
	v_lshrrev_b32_e32 v4, 4, v0
	v_and_b32_e32 v5, 6, v5
	v_and_or_b32 v4, v4, 8, v5
	v_lshrrev_b32_e32 v5, 8, v0
	v_or_b32_e32 v5, v5, v37
	s_waitcnt vmcnt(21)
	v_cvt_f16_f32_e32 v6, v20
	v_lshlrev_b32_e32 v5, 10, v5
	v_lshlrev_b32_e32 v3, 4, v3
	v_or3_b32 v3, v3, v5, v4
	v_cvt_f16_f32_e32 v4, v21
	v_cvt_f16_f32_e32 v5, v22
	v_add_u32_e32 v3, 0x10a00, v3
	v_cvt_f16_f32_e32 v7, v23
	s_waitcnt vmcnt(20)
	v_cvt_f16_f32_e32 v4, v24
	v_cvt_f16_f32_e32 v5, v25
	v_cvt_f16_f32_e32 v6, v26
	v_cvt_f16_f32_e32 v7, v27
	s_waitcnt vmcnt(19)
	v_cvt_f16_f32_e32 v4, v28
	v_cvt_f16_f32_e32 v5, v29
	v_cvt_f16_f32_e32 v6, v30
	v_cvt_f16_f32_e32 v7, v31
	s_waitcnt vmcnt(18)
	v_cvt_f16_f32_e32 v4, v32
	v_cvt_f16_f32_e32 v5, v33
	v_cvt_f16_f32_e32 v6, v34
	v_ashrrev_i32_e32 v43, 31, v42
	v_cvt_f16_f32_e32 v7, v35
	v_lshlrev_b64 v[4:5], 9, v[42:43]
	v_lshl_add_u64 v[4:5], s[12:13], 0, v[4:5]
	s_waitcnt lgkmcnt(0)
	s_barrier
	v_lshl_add_u64 v[4:5], v[4:5], 0, v[194:195]
	global_load_dwordx4 v[158:161], v[4:5], off
	global_load_dwordx4 v[154:157], v[4:5], off offset:64
	global_load_dwordx4 v[150:153], v[4:5], off offset:128
	global_load_dwordx4 v[146:149], v[4:5], off offset:192
	global_load_dwordx4 v[126:129], v[4:5], off offset:256
	global_load_dwordx4 v[114:117], v[4:5], off offset:320
	global_load_dwordx4 v[106:109], v[4:5], off offset:384
	global_load_dwordx4 v[98:101], v[4:5], off offset:448
	v_add_u32_e32 v2, 0xa0, v2
	v_ashrrev_i32_e32 v3, 31, v2
	v_lshl_add_u64 v[2:3], v[2:3], 2, s[8:9]
	global_load_dword v178, v[2:3], off
	v_lshlrev_b32_e32 v10, 4, v1
	v_add_u32_e32 v11, 0xca00, v10
	ds_read_b128 v[30:33], v10 offset:51712
	ds_read_b128 v[22:25], v10 offset:52736
	ds_read_b128 v[18:21], v10 offset:53760
	ds_read_b128 v[14:17], v10 offset:54784
	ds_read_b128 v[46:49], v10 offset:55808
	ds_read_b128 v[34:37], v10 offset:56832
	ds_read_b128 v[26:29], v10 offset:57856
	ds_read_b128 v[2:5], v10 offset:58880
	ds_read_b128 v[54:57], v10 offset:59904
	ds_read_b128 v[50:53], v10 offset:60928
	ds_read_b128 v[38:41], v10 offset:61952
	ds_read_b128 v[6:9], v10 offset:62976
	ds_read_b128 v[62:65], v10 offset:64000
	ds_read_b128 v[58:61], v10 offset:65024
	ds_read_b128 v[42:45], v11 offset:14336
	ds_read_b128 v[10:13], v11 offset:15360
	s_waitcnt vmcnt(26)
	v_cvt_pk_f16_f32 v82, v66, v67
	v_cvt_pk_f16_f32 v83, v68, v69
	s_waitcnt vmcnt(25)
	v_cvt_pk_f16_f32 v84, v70, v71
	v_cvt_pk_f16_f32 v85, v72, v73
	s_cselect_b64 s[4:5], -1, 0
	s_cmp_lg_u32 s33, 0
	v_mov_b64_e32 v[66:67], v[82:83]
	s_waitcnt vmcnt(24)
	v_cvt_pk_f16_f32 v78, v74, v75
	v_cvt_pk_f16_f32 v79, v76, v77
	s_waitcnt vmcnt(23)
	v_cvt_pk_f16_f32 v80, v102, v103
	v_cvt_pk_f16_f32 v81, v104, v105
	s_waitcnt vmcnt(22)
	v_cvt_pk_f16_f32 v74, v110, v111
	v_cvt_pk_f16_f32 v75, v112, v113
	s_waitcnt vmcnt(21)
	v_cvt_pk_f16_f32 v76, v162, v163
	v_cvt_pk_f16_f32 v77, v164, v165
	s_waitcnt vmcnt(20)
	v_cvt_pk_f16_f32 v70, v166, v167
	v_cvt_pk_f16_f32 v71, v168, v169
	s_waitcnt vmcnt(19)
	v_cvt_pk_f16_f32 v72, v170, v171
	v_cvt_pk_f16_f32 v73, v172, v173
	s_cselect_b64 s[10:11], -1, 0
	s_and_b64 vcc, exec, s[4:5]
	v_mov_b64_e32 v[68:69], v[84:85]
	s_cbranch_vccnz .LBB0_55
	s_cmp_eq_u32 s33, 1
	s_cselect_b64 vcc, -1, 0
	s_cmp_eq_u32 s33, 2
	s_cselect_b64 s[6:7], -1, 0
	v_cndmask_b32_e64 v66, v70, v74, s[6:7]
	v_cndmask_b32_e64 v67, v71, v75, s[6:7]
	v_cndmask_b32_e64 v68, v72, v76, s[6:7]
	v_cndmask_b32_e64 v69, v73, v77, s[6:7]
	v_cndmask_b32_e32 v69, v69, v81, vcc
	v_cndmask_b32_e32 v68, v68, v80, vcc
	v_cndmask_b32_e32 v67, v67, v79, vcc
	v_cndmask_b32_e32 v66, v66, v78, vcc

.LBB0_82:
	s_and_b32 s0, s2, 3
	s_lshl_b32 s0, s0, s4
	v_or3_b32 v13, v14, s0, v13
	s_ashr_i32 s0, s2, 1
	s_and_b32 s0, s0, -16
	v_lshrrev_b32_e32 v11, 3, v0
	v_lshl_add_u32 v13, v13, 7, s0
	v_and_or_b32 v14, v11, 15, v13
	v_mov_b32_e32 v16, s16
	v_mov_b32_e32 v17, s17
	v_ashrrev_i32_e32 v15, 31, v14
	v_lshl_add_u64 v[14:15], v[14:15], 2, v[16:17]
	global_load_dword v13, v[14:15], off
	s_lshl_b32 s4, s33, 5
	v_cmp_gt_u32_e32 vcc, 32, v0
	s_and_saveexec_b64 s[0:1], vcc
	v_mov_b32_e32 v14, 0x14a00
	v_lshl_add_u32 v14, v0, 2, v14
	v_mov_b32_e32 v15, 0
	ds_write_b32 v14, v15
	s_or_b64 exec, exec, s[0:1]
	v_add_u32_e32 v122, 0x100, v0
	v_mov_b32_e32 v109, 0
	v_lshlrev_b32_e32 v108, 4, v122
	v_lshl_add_u64 v[74:75], s[34:35], 0, v[108:109]
	v_add_co_u32_e32 v88, vcc, 0x2000, v74
	global_load_dwordx4 v[76:79], v108, s[34:35]
	s_nop 0
	v_addc_co_u32_e32 v89, vcc, 0, v75, vcc
	v_add_co_u32_e32 v90, vcc, 0x4000, v74
	s_mov_b32 s1, 0
	s_nop 0
	v_addc_co_u32_e32 v91, vcc, 0, v75, vcc
	v_add_co_u32_e32 v74, vcc, 0x6000, v74
	global_load_dwordx4 v[80:83], v[88:89], off
	global_load_dwordx4 v[84:87], v[90:91], off
	v_addc_co_u32_e32 v75, vcc, 0, v75, vcc
	global_load_dwordx4 v[88:91], v[74:75], off
	v_lshlrev_b32_e32 v74, 6, v122
	v_and_b32_e32 v74, 0x7e00, v74
	v_mov_b32_e32 v75, v109
	v_lshl_add_u64 v[92:93], s[18:19], 0, v[74:75]
	s_lshl_b32 s0, s4, 2
	v_lshl_add_u64 v[92:93], v[92:93], 0, s[0:1]
	v_and_b32_e32 v104, 0x70, v108
	v_mov_b32_e32 v105, v109
	v_lshl_add_u64 v[92:93], v[92:93], 0, v[104:105]
	v_or_b32_e32 v106, 0x8000, v74
	v_mov_b32_e32 v107, v109
	global_load_dwordx4 v[92:95], v[92:93], off
	v_lshl_add_u64 v[96:97], s[18:19], 0, v[106:107]
	v_lshl_add_u64 v[74:75], s[22:23], 0, v[74:75]
	v_lshl_add_u64 v[96:97], v[96:97], 0, s[0:1]
	v_lshl_add_u64 v[74:75], v[74:75], 0, s[0:1]
	v_lshl_add_u64 v[96:97], v[96:97], 0, v[104:105]
	v_lshl_add_u64 v[74:75], v[74:75], 0, v[104:105]
	global_load_dwordx4 v[96:99], v[96:97], off
	v_lshlrev_b32_e32 v109, 3, v122
	global_load_dwordx4 v[100:103], v[74:75], off
	v_lshl_add_u64 v[74:75], s[22:23], 0, v[106:107]
	v_lshl_add_u64 v[74:75], v[74:75], 0, s[0:1]
	v_lshl_add_u64 v[74:75], v[74:75], 0, v[104:105]
	global_load_dwordx4 v[104:107], v[74:75], off
	v_mov_b32_e32 v49, 0
	v_lshlrev_b32_e32 v48, 4, v0
	v_lshl_add_u64 v[14:15], s[34:35], 0, v[48:49]
	v_add_co_u32_e32 v28, vcc, 0x2000, v14
	global_load_dwordx4 v[16:19], v48, s[34:35]
	s_nop 0
	v_addc_co_u32_e32 v29, vcc, 0, v15, vcc
	v_add_co_u32_e32 v30, vcc, 0x4000, v14
	s_mov_b32 s1, 0
	s_nop 0
	v_addc_co_u32_e32 v31, vcc, 0, v15, vcc
	v_add_co_u32_e32 v14, vcc, 0x6000, v14
	global_load_dwordx4 v[20:23], v[28:29], off
	global_load_dwordx4 v[24:27], v[30:31], off
	v_addc_co_u32_e32 v15, vcc, 0, v15, vcc
	global_load_dwordx4 v[28:31], v[14:15], off
	v_lshlrev_b32_e32 v14, 6, v0
	v_and_b32_e32 v14, 0x7e00, v14
	v_mov_b32_e32 v15, v49
	v_lshl_add_u64 v[32:33], s[18:19], 0, v[14:15]
	s_lshl_b32 s0, s4, 2
	v_lshl_add_u64 v[32:33], v[32:33], 0, s[0:1]
	v_and_b32_e32 v44, 0x70, v48
	v_mov_b32_e32 v45, v49
	v_lshl_add_u64 v[32:33], v[32:33], 0, v[44:45]
	v_or_b32_e32 v46, 0x8000, v14
	v_mov_b32_e32 v47, v49
	global_load_dwordx4 v[32:35], v[32:33], off
	v_lshl_add_u64 v[36:37], s[18:19], 0, v[46:47]
	v_lshl_add_u64 v[14:15], s[22:23], 0, v[14:15]
	v_lshl_add_u64 v[36:37], v[36:37], 0, s[0:1]
	v_lshl_add_u64 v[14:15], v[14:15], 0, s[0:1]
	v_lshl_add_u64 v[36:37], v[36:37], 0, v[44:45]
	v_lshl_add_u64 v[14:15], v[14:15], 0, v[44:45]
	global_load_dwordx4 v[36:39], v[36:37], off
	v_lshlrev_b32_e32 v49, 3, v0
	global_load_dwordx4 v[40:43], v[14:15], off
	v_lshl_add_u64 v[14:15], s[22:23], 0, v[46:47]
	v_lshl_add_u64 v[14:15], v[14:15], 0, s[0:1]
	v_lshl_add_u64 v[14:15], v[14:15], 0, v[44:45]
	global_load_dwordx4 v[44:47], v[14:15], off
	v_lshrrev_b32_e32 v110, 1, v122
	v_lshrrev_b32_e32 v75, 5, v122
	v_and_b32_e32 v74, 4, v122
	v_lshrrev_b32_e32 v112, 2, v122
	v_lshrrev_b32_e32 v113, 8, v122
	v_and_b32_e32 v108, 48, v108
	v_and_b32_e32 v109, 0xc0, v109
	v_and_b32_e32 v110, 48, v110
	v_lshrrev_b32_e32 v111, 4, v122
	v_lshlrev_b32_e32 v114, 1, v74
	v_and_b32_e32 v112, 6, v112
	v_or_b32_e32 v113, v113, v74
	v_or3_b32 v75, v108, v75, v109
	v_and_or_b32 v108, v10, 12, v110
	v_and_or_b32 v109, v111, 8, v112
	v_lshlrev_b32_e32 v110, 10, v113
	v_lshl_or_b32 v75, v75, 4, v114
	v_lshlrev_b32_e32 v108, 4, v108
	v_or3_b32 v108, v110, v108, v109
	v_add_u32_e32 v108, 0x10a00, v108
	v_lshrrev_b32_e32 v50, 1, v0
	v_lshrrev_b32_e32 v15, 5, v0
	v_and_b32_e32 v14, 4, v0
	v_lshrrev_b32_e32 v52, 2, v0
	v_lshrrev_b32_e32 v53, 8, v0
	v_and_b32_e32 v48, 48, v48
	v_and_b32_e32 v49, 0xc0, v49
	v_and_b32_e32 v50, 48, v50
	v_lshrrev_b32_e32 v51, 4, v0
	v_lshlrev_b32_e32 v54, 1, v14
	v_and_b32_e32 v52, 6, v52
	v_or_b32_e32 v53, v53, v14
	v_or3_b32 v15, v48, v15, v49
	v_and_or_b32 v48, v10, 12, v50
	v_and_or_b32 v49, v51, 8, v52
	v_lshlrev_b32_e32 v50, 10, v53
	v_lshl_or_b32 v15, v15, 4, v54
	v_lshlrev_b32_e32 v48, 4, v48
	v_or3_b32 v48, v50, v48, v49
	v_add_u32_e32 v48, 0x10a00, v48
	s_movk_i32 s0, 0x80
	v_cmp_gt_u32_e32 vcc, s0, v0
	s_waitcnt vmcnt(15)
	v_cvt_pk_f16_f32 v76, v76, v77
	v_cvt_pk_f16_f32 v77, v78, v79
	s_waitcnt vmcnt(14)
	v_cvt_pk_f16_f32 v78, v80, v81
	v_cvt_pk_f16_f32 v79, v82, v83
	ds_write2st64_b64 v75, v[76:77], v[78:79] offset0:101 offset1:109
	s_waitcnt vmcnt(13)
	v_cvt_pk_f16_f32 v76, v84, v85
	v_cvt_pk_f16_f32 v77, v86, v87
	s_waitcnt vmcnt(12)
	v_cvt_pk_f16_f32 v78, v88, v89
	v_cvt_pk_f16_f32 v79, v90, v91
	s_waitcnt vmcnt(11)
	v_cvt_f16_f32_e32 v80, v92
	v_cvt_f16_f32_e32 v81, v93
	v_cvt_f16_f32_e32 v82, v94
	v_cvt_f16_f32_e32 v83, v95
	s_waitcnt vmcnt(10)
	v_cvt_f16_f32_e32 v84, v96
	v_cvt_f16_f32_e32 v85, v97
	v_cvt_f16_f32_e32 v86, v98
	v_cvt_f16_f32_e32 v87, v99
	ds_write2st64_b64 v75, v[76:77], v[78:79] offset0:117 offset1:125
	ds_write_b16 v108, v80
	ds_write_b16 v108, v81 offset:16
	ds_write_b16 v108, v82 offset:32
	ds_write_b16 v108, v83 offset:48
	ds_write_b16 v108, v84 offset:2048
	ds_write_b16 v108, v85 offset:2064
	ds_write_b16 v108, v86 offset:2080
	ds_write_b16 v108, v87 offset:2096
	s_waitcnt vmcnt(9)
	v_cvt_f16_f32_e32 v75, v100
	v_cvt_f16_f32_e32 v76, v101
	v_cvt_f16_f32_e32 v77, v102
	v_cvt_f16_f32_e32 v78, v103
	ds_write_b16 v108, v75 offset:8192
	ds_write_b16 v108, v76 offset:8208
	ds_write_b16 v108, v77 offset:8224
	ds_write_b16 v108, v78 offset:8240
	s_waitcnt vmcnt(8)
	v_cvt_f16_f32_e32 v75, v104
	v_cvt_f16_f32_e32 v76, v105
	v_cvt_f16_f32_e32 v77, v106
	v_cvt_f16_f32_e32 v78, v107
	ds_write_b16 v108, v75 offset:10240
	ds_write_b16 v108, v76 offset:10256
	ds_write_b16 v108, v77 offset:10272
	ds_write_b16 v108, v78 offset:10288
	s_waitcnt vmcnt(7)
	v_cvt_pk_f16_f32 v16, v16, v17
	v_cvt_pk_f16_f32 v17, v18, v19
	s_waitcnt vmcnt(6)
	v_cvt_pk_f16_f32 v18, v20, v21
	v_cvt_pk_f16_f32 v19, v22, v23
	ds_write2st64_b64 v15, v[16:17], v[18:19] offset0:101 offset1:109
	s_waitcnt vmcnt(5)
	v_cvt_pk_f16_f32 v16, v24, v25
	v_cvt_pk_f16_f32 v17, v26, v27
	s_waitcnt vmcnt(4)
	v_cvt_pk_f16_f32 v18, v28, v29
	v_cvt_pk_f16_f32 v19, v30, v31
	s_waitcnt vmcnt(3)
	v_cvt_f16_f32_e32 v20, v32
	v_cvt_f16_f32_e32 v21, v33
	v_cvt_f16_f32_e32 v22, v34
	v_cvt_f16_f32_e32 v23, v35
	s_waitcnt vmcnt(2)
	v_cvt_f16_f32_e32 v24, v36
	v_cvt_f16_f32_e32 v25, v37
	v_cvt_f16_f32_e32 v26, v38
	v_cvt_f16_f32_e32 v27, v39
	ds_write2st64_b64 v15, v[16:17], v[18:19] offset0:117 offset1:125
	ds_write_b16 v48, v20
	ds_write_b16 v48, v21 offset:16
	ds_write_b16 v48, v22 offset:32
	ds_write_b16 v48, v23 offset:48
	ds_write_b16 v48, v24 offset:2048
	ds_write_b16 v48, v25 offset:2064
	ds_write_b16 v48, v26 offset:2080
	ds_write_b16 v48, v27 offset:2096
	s_waitcnt vmcnt(1)
	v_cvt_f16_f32_e32 v15, v40
	v_cvt_f16_f32_e32 v16, v41
	v_cvt_f16_f32_e32 v17, v42
	v_cvt_f16_f32_e32 v18, v43
	ds_write_b16 v48, v15 offset:8192
	ds_write_b16 v48, v16 offset:8208
	ds_write_b16 v48, v17 offset:8224
	ds_write_b16 v48, v18 offset:8240
	s_waitcnt vmcnt(0)
	v_cvt_f16_f32_e32 v15, v44
	v_cvt_f16_f32_e32 v16, v45
	v_cvt_f16_f32_e32 v17, v46
	v_cvt_f16_f32_e32 v18, v47
	ds_write_b16 v48, v15 offset:10240
	ds_write_b16 v48, v16 offset:10256
	ds_write_b16 v48, v17 offset:10272
	ds_write_b16 v48, v18 offset:10288
	s_and_saveexec_b64 s[0:1], vcc
	s_cbranch_execz .LBB0_86
	v_cvt_f16_f32_e32 v13, v13
	v_lshl_or_b32 v18, s2, 7, v0
	v_mov_b32_e32 v16, s28
	v_mov_b32_e32 v17, s29
	v_ashrrev_i32_e32 v19, 31, v18
	v_lshl_add_u64 v[16:17], v[18:19], 1, v[16:17]
	global_store_short v[16:17], v13, off
